# GEMM setprio flips removed plus one static s_setprio 1 for waves 0-3 at kernel start
# speedup vs baseline: 1.0119x; 1.0038x over previous
; #define LAS __attribute__((address_space(3)))
; __device__ __forceinline__ float siluf_(float x) { return x * sigmoidf_(x); }
; __device__ __forceinline__ Frame fresh(const Frame& F0) { Frame F = F0; int ln = lane_id_(); asm volatile("" : "+v"(ln)); F.lane = ln; F.tid = F0.wave * 64 + ln; return F; }
; #define SEAM(k) do { if (IN(k) && IN((k) + 1)) { xcd_barrier(bar); if (REPM & 1) xcd_barrier(bar); } } while (0)
; __device__ __forceinline__ void ph_mods(const Frame& F) {
;     const float* c = inp(F, 1); const float* cc = inp(F, 3); const float* ada_w = inp(F, 4); const float* ada_b = inp(F, 5);
;     LAS float* sv = (LAS float*)F.lds;
;     LAS float* red = (LAS float*)(F.lds + 5 * 1024 * 4);
;     for (int i = F.tid; i < 5 * 1024; i += 512) { const int s = i >> 10, k = i & 1023; const float v = (s < 4) ? c[s * 1024 + k] : cc[k]; sv[i] = siluf_(v); }
; __global__ void __launch_bounds__(512, 2) mk_fwd(Args args) {
;     extern __shared__ __attribute__((aligned(16))) unsigned char lds_raw[];
;     Frame F;
;     F.out = args.out; F.ws = args.ws; F.lds = (LAS unsigned char*)lds_raw;
;     { const int t0 = threadIdx.x; F.wave = __builtin_amdgcn_readfirstlane(t0 >> 6); F.lane = t0 & 63; F.tid = t0; } F.G = gridDim.x; F.wg = blockIdx.x;
;     F.mods = (float*)(args.ws + OFF_MODS); F.X = (float*)(args.ws + OFF_X); F.HB = (bf16_t*)(args.ws + OFF_HB); F.MIX = F.HB;
;     F.WB = args.ws + OFF_WB; F.R1 = args.ws + OFF_R1;
;     volatile LAS unsigned* xbw = (volatile LAS unsigned*)(F.lds + LDS_MISC);
;     if (F.tid < 4) xbw[F.tid] = 0u;
;     if (F.tid < 30) ((LAS unsigned long long*)(F.lds + LDS_MISC + MISC_INP))[F.tid] = (unsigned long long)args.in[F.tid];
;     __syncthreads();
;     const int lo = args.ph_lo, hi = args.ph_hi;
;     XcdBarrier bar; bar.bar = (unsigned*)(args.ws + OFF_CTL); bar.x = 0; bar.st = xbw;
;     if (hi - lo > 1) bar = xcd_barrier_post((unsigned*)(args.ws + OFF_CTL), xbw);
;     ...
;     if ((PHM & 1) && IN(0)) { ph_mods(fresh(F)); if (REPM & 65536) { __syncthreads(); ph_mods(fresh(F)); } } SEAM(0);
.LBB0_9:
	s_lshr_b32 s75, s2, 6
	s_cmp_ge_u32 s75, 4
	s_cbranch_scc1 .Lprio_static_done
	s_setprio 1
.Lprio_static_done:
	s_add_u32 s28, s62, 0x10000
	s_addc_u32 s29, s63, 0
	s_cmp_lt_i32 s40, 1
	s_cselect_b64 s[4:5], -1, 0
	s_cmp_gt_i32 s40, 0
	s_cselect_b64 s[0:1], -1, 0
	s_cmp_lt_i32 s41, 1
	s_cselect_b64 s[6:7], -1, 0
	s_or_b64 s[0:1], s[0:1], s[6:7]
	s_and_b64 vcc, exec, s[0:1]
	v_mbcnt_lo_u32_b32 v1, -1, 0
	s_cbranch_vccnz .LBB0_25
	s_add_i32 s1, 0, 0x20908
	v_mbcnt_hi_u32_b32 v51, -1, v1
	v_mov_b32_e32 v2, s1
	ds_read_b64 v[6:7], v2
	s_and_b32 s0, s2, 0xffffffc0
	v_add_u32_e32 v48, s0, v51
	s_add_i32 s0, 0, 0x20918
	v_mov_b32_e32 v2, s0
	s_add_i32 s0, 0, 0x20928
	s_waitcnt lgkmcnt(0)
	v_readfirstlane_b32 s12, v6
	v_mov_b32_e32 v6, s0
	ds_read2_b64 v[2:5], v2 offset1:1
	v_readfirstlane_b32 s13, v7
	ds_read_b64 v[6:7], v6
	s_movk_i32 s10, 0x1400
	v_cmp_gt_i32_e32 vcc, s10, v48
	s_waitcnt lgkmcnt(1)
	v_readfirstlane_b32 s9, v3
	v_readfirstlane_b32 s8, v2
	v_readfirstlane_b32 s1, v5
	v_readfirstlane_b32 s0, v4
	s_waitcnt lgkmcnt(0)
	v_readfirstlane_b32 s7, v7
	v_readfirstlane_b32 s6, v6
	s_and_saveexec_b64 s[10:11], vcc
	s_cbranch_execz .LBB0_13
	s_lshl_b32 s14, s75, 8
	s_add_i32 s14, s14, 0
	v_ashrrev_i32_e32 v49, 31, v48
	v_lshl_add_u32 v6, v51, 2, s14
	v_lshl_add_u64 v[2:3], v[48:49], 2, s[12:13]
	s_mov_b64 s[12:13], 0
	s_movk_i32 s16, 0x1000
	v_mov_b32_e32 v5, 0
	s_mov_b64 s[14:15], 0x800
	s_movk_i32 s17, 0x11ff
	v_mov_b32_e32 v7, v48
